# O1: out-proj epilogue rewritten as two straight-line variants (f32 / bf16 residual) with 6 rotating buffers: residual loads run 5 pieces ahead of the fma/cvt/store, counted vmcnt; on top of T1-T3+G2+B
# speedup vs baseline: 1.0116x; 1.0005x over previous
.LBB0_1005:
	s_ashr_i32 s4, s44, 31
	s_lshr_b32 s4, s4, 20
	s_add_i32 s4, s44, s4
	s_ashr_i32 s4, s4, 12
	s_mul_hi_i32 s5, s4, 0xc000
	s_mul_i32 s4, s4, 0xc000
	v_lshl_or_b32 v166, s45, 8, v182
	s_add_u32 s4, s38, s4
	s_addc_u32 s5, s39, s5
	v_ashrrev_i32_e32 v167, 31, v166
	v_lshl_add_u64 v[76:77], v[166:167], 2, s[4:5]
	global_load_dwordx4 v[80:83], v[76:77], off offset:16
	global_load_dwordx4 v[84:87], v[76:77], off
	global_load_dwordx4 v[68:71], v[76:77], off offset:528
	s_nop 0
	global_load_dwordx4 v[76:79], v[76:77], off offset:512
	v_add_u32_e32 v172, s44, v180
	v_ashrrev_i32_e32 v173, 31, v172
	v_lshlrev_b64 v[144:145], 11, v[172:173]
	v_lshl_add_u64 v[178:179], v[144:145], 0, v[166:167]
	v_cndmask_b32_e64 v144, 0, 1, s[8:9]
	v_cmp_ne_u32_e64 s[4:5], 1, v144
	s_andn2_b64 vcc, exec, s[8:9]
	v_lshl_add_u64 v[176:177], v[178:179], 1, s[10:11]
	s_and_b64 vcc, exec, s[8:9]
	s_cbranch_vccz .LO1_f32
	v_mov_b32_e32 v184, v178
	v_mov_b32_e32 v185, v179
	v_mov_b32_e32 v188, v178
	v_mov_b32_e32 v189, v179
	v_lshl_add_u64 v[174:175], v[184:185], 1, s[10:11]
	global_load_dwordx4 v[148:151], v[174:175], off
	global_load_dwordx4 v[212:215], v[174:175], off offset:256
	s_mov_b64 s[98:99], 0x8000
	v_lshl_add_u64 v[184:185], v[184:185], 0, s[98:99]
	v_lshl_add_u64 v[174:175], v[184:185], 1, s[10:11]
	global_load_dwordx4 v[220:223], v[174:175], off
	global_load_dwordx4 v[228:231], v[174:175], off offset:256
	s_mov_b64 s[98:99], 0x8000
	v_lshl_add_u64 v[184:185], v[184:185], 0, s[98:99]
	v_lshl_add_u64 v[174:175], v[184:185], 1, s[10:11]
	global_load_dwordx4 v[236:239], v[174:175], off
	s_waitcnt vmcnt(4)
	v_lshlrev_b32_e32 v144, 16, v148
	v_and_b32_e32 v145, 0xffff0000, v148
	v_lshlrev_b32_e32 v146, 16, v149
	v_and_b32_e32 v147, 0xffff0000, v149
	v_lshlrev_b32_e32 v148, 16, v150
	v_and_b32_e32 v149, 0xffff0000, v150
	v_lshlrev_b32_e32 v150, 16, v151
	v_and_b32_e32 v151, 0xffff0000, v151
	v_pk_fma_f32 v[144:145], v[140:141], v[84:85], v[144:145]
	v_pk_fma_f32 v[146:147], v[142:143], v[86:87], v[146:147]
	v_pk_fma_f32 v[148:149], v[136:137], v[80:81], v[148:149]
	v_pk_fma_f32 v[150:151], v[138:139], v[82:83], v[150:151]
	v_lshl_add_u64 v[176:177], v[188:189], 1, s[12:13]
	v_cvt_pk_bf16_f32 v144, v144, v145
	v_cvt_pk_bf16_f32 v145, v146, v147
	v_cvt_pk_bf16_f32 v146, v148, v149
	v_cvt_pk_bf16_f32 v147, v150, v151
	global_store_dwordx4 v[176:177], v[144:147], off
	global_load_dwordx4 v[244:247], v[174:175], off offset:256
	s_waitcnt vmcnt(5)
	v_lshlrev_b32_e32 v208, 16, v212
	v_and_b32_e32 v209, 0xffff0000, v212
	v_lshlrev_b32_e32 v210, 16, v213
	v_and_b32_e32 v211, 0xffff0000, v213
	v_lshlrev_b32_e32 v212, 16, v214
	v_and_b32_e32 v213, 0xffff0000, v214
	v_lshlrev_b32_e32 v214, 16, v215
	v_and_b32_e32 v215, 0xffff0000, v215
	v_pk_fma_f32 v[208:209], v[132:133], v[76:77], v[208:209]
	v_pk_fma_f32 v[210:211], v[134:135], v[78:79], v[210:211]
	v_pk_fma_f32 v[212:213], v[128:129], v[68:69], v[212:213]
	v_pk_fma_f32 v[214:215], v[130:131], v[70:71], v[214:215]
	v_cvt_pk_bf16_f32 v208, v208, v209
	v_cvt_pk_bf16_f32 v209, v210, v211
	v_cvt_pk_bf16_f32 v210, v212, v213
	v_cvt_pk_bf16_f32 v211, v214, v215
	global_store_dwordx4 v[176:177], v[208:211], off offset:256
	s_mov_b64 s[98:99], 0x8000
	v_lshl_add_u64 v[184:185], v[184:185], 0, s[98:99]
	v_lshl_add_u64 v[174:175], v[184:185], 1, s[10:11]
	global_load_dwordx4 v[148:151], v[174:175], off
	s_waitcnt vmcnt(6)
	v_lshlrev_b32_e32 v216, 16, v220
	v_and_b32_e32 v217, 0xffff0000, v220
	v_lshlrev_b32_e32 v218, 16, v221
	v_and_b32_e32 v219, 0xffff0000, v221
	v_lshlrev_b32_e32 v220, 16, v222
	v_and_b32_e32 v221, 0xffff0000, v222
	v_lshlrev_b32_e32 v222, 16, v223
	v_and_b32_e32 v223, 0xffff0000, v223
	v_pk_fma_f32 v[216:217], v[124:125], v[84:85], v[216:217]
	v_pk_fma_f32 v[218:219], v[126:127], v[86:87], v[218:219]
	v_pk_fma_f32 v[220:221], v[120:121], v[80:81], v[220:221]
	v_pk_fma_f32 v[222:223], v[122:123], v[82:83], v[222:223]
	s_mov_b64 s[98:99], 0x8000
	v_lshl_add_u64 v[188:189], v[188:189], 0, s[98:99]
	v_lshl_add_u64 v[176:177], v[188:189], 1, s[12:13]
	v_cvt_pk_bf16_f32 v216, v216, v217
	v_cvt_pk_bf16_f32 v217, v218, v219
	v_cvt_pk_bf16_f32 v218, v220, v221
	v_cvt_pk_bf16_f32 v219, v222, v223
	global_store_dwordx4 v[176:177], v[216:219], off
	global_load_dwordx4 v[212:215], v[174:175], off offset:256
	s_waitcnt vmcnt(7)
	v_lshlrev_b32_e32 v224, 16, v228
	v_and_b32_e32 v225, 0xffff0000, v228
	v_lshlrev_b32_e32 v226, 16, v229
	v_and_b32_e32 v227, 0xffff0000, v229
	v_lshlrev_b32_e32 v228, 16, v230
	v_and_b32_e32 v229, 0xffff0000, v230
	v_lshlrev_b32_e32 v230, 16, v231
	v_and_b32_e32 v231, 0xffff0000, v231
	v_pk_fma_f32 v[224:225], v[116:117], v[76:77], v[224:225]
	v_pk_fma_f32 v[226:227], v[118:119], v[78:79], v[226:227]
	v_pk_fma_f32 v[228:229], v[112:113], v[68:69], v[228:229]
	v_pk_fma_f32 v[230:231], v[114:115], v[70:71], v[230:231]
	v_cvt_pk_bf16_f32 v224, v224, v225
	v_cvt_pk_bf16_f32 v225, v226, v227
	v_cvt_pk_bf16_f32 v226, v228, v229
	v_cvt_pk_bf16_f32 v227, v230, v231
	global_store_dwordx4 v[176:177], v[224:227], off offset:256
	s_mov_b64 s[98:99], 0x28000
	v_lshl_add_u64 v[184:185], v[184:185], 0, s[98:99]
	v_lshl_add_u64 v[174:175], v[184:185], 1, s[10:11]
	global_load_dwordx4 v[220:223], v[174:175], off
	s_waitcnt vmcnt(8)
	v_lshlrev_b32_e32 v232, 16, v236
	v_and_b32_e32 v233, 0xffff0000, v236
	v_lshlrev_b32_e32 v234, 16, v237
	v_and_b32_e32 v235, 0xffff0000, v237
	v_lshlrev_b32_e32 v236, 16, v238
	v_and_b32_e32 v237, 0xffff0000, v238
	v_lshlrev_b32_e32 v238, 16, v239
	v_and_b32_e32 v239, 0xffff0000, v239
	v_pk_fma_f32 v[232:233], v[108:109], v[84:85], v[232:233]
	v_pk_fma_f32 v[234:235], v[110:111], v[86:87], v[234:235]
	v_pk_fma_f32 v[236:237], v[104:105], v[80:81], v[236:237]
	v_pk_fma_f32 v[238:239], v[106:107], v[82:83], v[238:239]
	s_mov_b64 s[98:99], 0x8000
	v_lshl_add_u64 v[188:189], v[188:189], 0, s[98:99]
	v_lshl_add_u64 v[176:177], v[188:189], 1, s[12:13]
	v_cvt_pk_bf16_f32 v232, v232, v233
	v_cvt_pk_bf16_f32 v233, v234, v235
	v_cvt_pk_bf16_f32 v234, v236, v237
	v_cvt_pk_bf16_f32 v235, v238, v239
	global_store_dwordx4 v[176:177], v[232:235], off
	global_load_dwordx4 v[228:231], v[174:175], off offset:256
	s_waitcnt vmcnt(8)
	v_lshlrev_b32_e32 v240, 16, v244
	v_and_b32_e32 v241, 0xffff0000, v244
	v_lshlrev_b32_e32 v242, 16, v245
	v_and_b32_e32 v243, 0xffff0000, v245
	v_lshlrev_b32_e32 v244, 16, v246
	v_and_b32_e32 v245, 0xffff0000, v246
	v_lshlrev_b32_e32 v246, 16, v247
	v_and_b32_e32 v247, 0xffff0000, v247
	v_pk_fma_f32 v[240:241], v[100:101], v[76:77], v[240:241]
	v_pk_fma_f32 v[242:243], v[102:103], v[78:79], v[242:243]
	v_pk_fma_f32 v[244:245], v[96:97], v[68:69], v[244:245]
	v_pk_fma_f32 v[246:247], v[98:99], v[70:71], v[246:247]
	v_cvt_pk_bf16_f32 v240, v240, v241
	v_cvt_pk_bf16_f32 v241, v242, v243
	v_cvt_pk_bf16_f32 v242, v244, v245
	v_cvt_pk_bf16_f32 v243, v246, v247
	global_store_dwordx4 v[176:177], v[240:243], off offset:256
	s_mov_b64 s[98:99], 0x8000
	v_lshl_add_u64 v[184:185], v[184:185], 0, s[98:99]
	v_lshl_add_u64 v[174:175], v[184:185], 1, s[10:11]
	global_load_dwordx4 v[236:239], v[174:175], off
	s_waitcnt vmcnt(8)
	v_lshlrev_b32_e32 v144, 16, v148
	v_and_b32_e32 v145, 0xffff0000, v148
	v_lshlrev_b32_e32 v146, 16, v149
	v_and_b32_e32 v147, 0xffff0000, v149
	v_lshlrev_b32_e32 v148, 16, v150
	v_and_b32_e32 v149, 0xffff0000, v150
	v_lshlrev_b32_e32 v150, 16, v151
	v_and_b32_e32 v151, 0xffff0000, v151
	v_pk_fma_f32 v[144:145], v[92:93], v[84:85], v[144:145]
	v_pk_fma_f32 v[146:147], v[94:95], v[86:87], v[146:147]
	v_pk_fma_f32 v[148:149], v[88:89], v[80:81], v[148:149]
	v_pk_fma_f32 v[150:151], v[90:91], v[82:83], v[150:151]
	s_mov_b64 s[98:99], 0x8000
	v_lshl_add_u64 v[188:189], v[188:189], 0, s[98:99]
	v_lshl_add_u64 v[176:177], v[188:189], 1, s[12:13]
	v_cvt_pk_bf16_f32 v144, v144, v145
	v_cvt_pk_bf16_f32 v145, v146, v147
	v_cvt_pk_bf16_f32 v146, v148, v149
	v_cvt_pk_bf16_f32 v147, v150, v151
	global_store_dwordx4 v[176:177], v[144:147], off
	global_load_dwordx4 v[244:247], v[174:175], off offset:256
	s_waitcnt vmcnt(8)
	v_lshlrev_b32_e32 v208, 16, v212
	v_and_b32_e32 v209, 0xffff0000, v212
	v_lshlrev_b32_e32 v210, 16, v213
	v_and_b32_e32 v211, 0xffff0000, v213
	v_lshlrev_b32_e32 v212, 16, v214
	v_and_b32_e32 v213, 0xffff0000, v214
	v_lshlrev_b32_e32 v214, 16, v215
	v_and_b32_e32 v215, 0xffff0000, v215
	v_pk_fma_f32 v[208:209], v[72:73], v[76:77], v[208:209]
	v_pk_fma_f32 v[210:211], v[74:75], v[78:79], v[210:211]
	v_pk_fma_f32 v[212:213], v[64:65], v[68:69], v[212:213]
	v_pk_fma_f32 v[214:215], v[66:67], v[70:71], v[214:215]
	v_cvt_pk_bf16_f32 v208, v208, v209
	v_cvt_pk_bf16_f32 v209, v210, v211
	v_cvt_pk_bf16_f32 v210, v212, v213
	v_cvt_pk_bf16_f32 v211, v214, v215
	global_store_dwordx4 v[176:177], v[208:211], off offset:256
	s_mov_b64 s[98:99], 0x8000
	v_lshl_add_u64 v[184:185], v[184:185], 0, s[98:99]
	v_lshl_add_u64 v[174:175], v[184:185], 1, s[10:11]
	global_load_dwordx4 v[148:151], v[174:175], off
	s_waitcnt vmcnt(8)
	v_lshlrev_b32_e32 v216, 16, v220
	v_and_b32_e32 v217, 0xffff0000, v220
	v_lshlrev_b32_e32 v218, 16, v221
	v_and_b32_e32 v219, 0xffff0000, v221
	v_lshlrev_b32_e32 v220, 16, v222
	v_and_b32_e32 v221, 0xffff0000, v222
	v_lshlrev_b32_e32 v222, 16, v223
	v_and_b32_e32 v223, 0xffff0000, v223
	v_pk_fma_f32 v[216:217], v[60:61], v[84:85], v[216:217]
	v_pk_fma_f32 v[218:219], v[62:63], v[86:87], v[218:219]
	v_pk_fma_f32 v[220:221], v[56:57], v[80:81], v[220:221]
	v_pk_fma_f32 v[222:223], v[58:59], v[82:83], v[222:223]
	s_mov_b64 s[98:99], 0x28000
	v_lshl_add_u64 v[188:189], v[188:189], 0, s[98:99]
	v_lshl_add_u64 v[176:177], v[188:189], 1, s[12:13]
	v_cvt_pk_bf16_f32 v216, v216, v217
	v_cvt_pk_bf16_f32 v217, v218, v219
	v_cvt_pk_bf16_f32 v218, v220, v221
	v_cvt_pk_bf16_f32 v219, v222, v223
	global_store_dwordx4 v[176:177], v[216:219], off
	global_load_dwordx4 v[212:215], v[174:175], off offset:256
	s_waitcnt vmcnt(8)
	v_lshlrev_b32_e32 v224, 16, v228
	v_and_b32_e32 v225, 0xffff0000, v228
	v_lshlrev_b32_e32 v226, 16, v229
	v_and_b32_e32 v227, 0xffff0000, v229
	v_lshlrev_b32_e32 v228, 16, v230
	v_and_b32_e32 v229, 0xffff0000, v230
	v_lshlrev_b32_e32 v230, 16, v231
	v_and_b32_e32 v231, 0xffff0000, v231
	v_pk_fma_f32 v[224:225], v[52:53], v[76:77], v[224:225]
	v_pk_fma_f32 v[226:227], v[54:55], v[78:79], v[226:227]
	v_pk_fma_f32 v[228:229], v[48:49], v[68:69], v[228:229]
	v_pk_fma_f32 v[230:231], v[50:51], v[70:71], v[230:231]
	v_cvt_pk_bf16_f32 v224, v224, v225
	v_cvt_pk_bf16_f32 v225, v226, v227
	v_cvt_pk_bf16_f32 v226, v228, v229
	v_cvt_pk_bf16_f32 v227, v230, v231
	global_store_dwordx4 v[176:177], v[224:227], off offset:256
	s_mov_b64 s[98:99], 0x8000
	v_lshl_add_u64 v[184:185], v[184:185], 0, s[98:99]
	v_lshl_add_u64 v[174:175], v[184:185], 1, s[10:11]
	global_load_dwordx4 v[220:223], v[174:175], off
	s_waitcnt vmcnt(8)
	v_lshlrev_b32_e32 v232, 16, v236
	v_and_b32_e32 v233, 0xffff0000, v236
	v_lshlrev_b32_e32 v234, 16, v237
	v_and_b32_e32 v235, 0xffff0000, v237
	v_lshlrev_b32_e32 v236, 16, v238
	v_and_b32_e32 v237, 0xffff0000, v238
	v_lshlrev_b32_e32 v238, 16, v239
	v_and_b32_e32 v239, 0xffff0000, v239
	v_pk_fma_f32 v[232:233], v[44:45], v[84:85], v[232:233]
	v_pk_fma_f32 v[234:235], v[46:47], v[86:87], v[234:235]
	v_pk_fma_f32 v[236:237], v[40:41], v[80:81], v[236:237]
	v_pk_fma_f32 v[238:239], v[42:43], v[82:83], v[238:239]
	s_mov_b64 s[98:99], 0x8000
	v_lshl_add_u64 v[188:189], v[188:189], 0, s[98:99]
	v_lshl_add_u64 v[176:177], v[188:189], 1, s[12:13]
	v_cvt_pk_bf16_f32 v232, v232, v233
	v_cvt_pk_bf16_f32 v233, v234, v235
	v_cvt_pk_bf16_f32 v234, v236, v237
	v_cvt_pk_bf16_f32 v235, v238, v239
	global_store_dwordx4 v[176:177], v[232:235], off
	global_load_dwordx4 v[228:231], v[174:175], off offset:256
	s_waitcnt vmcnt(8)
	v_lshlrev_b32_e32 v240, 16, v244
	v_and_b32_e32 v241, 0xffff0000, v244
	v_lshlrev_b32_e32 v242, 16, v245
	v_and_b32_e32 v243, 0xffff0000, v245
	v_lshlrev_b32_e32 v244, 16, v246
	v_and_b32_e32 v245, 0xffff0000, v246
	v_lshlrev_b32_e32 v246, 16, v247
	v_and_b32_e32 v247, 0xffff0000, v247
	v_pk_fma_f32 v[240:241], v[36:37], v[76:77], v[240:241]
	v_pk_fma_f32 v[242:243], v[38:39], v[78:79], v[242:243]
	v_pk_fma_f32 v[244:245], v[32:33], v[68:69], v[244:245]
	v_pk_fma_f32 v[246:247], v[34:35], v[70:71], v[246:247]
	v_cvt_pk_bf16_f32 v240, v240, v241
	v_cvt_pk_bf16_f32 v241, v242, v243
	v_cvt_pk_bf16_f32 v242, v244, v245
	v_cvt_pk_bf16_f32 v243, v246, v247
	global_store_dwordx4 v[176:177], v[240:243], off offset:256
	s_waitcnt vmcnt(7)
	v_lshlrev_b32_e32 v144, 16, v148
	v_and_b32_e32 v145, 0xffff0000, v148
	v_lshlrev_b32_e32 v146, 16, v149
	v_and_b32_e32 v147, 0xffff0000, v149
	v_lshlrev_b32_e32 v148, 16, v150
	v_and_b32_e32 v149, 0xffff0000, v150
	v_lshlrev_b32_e32 v150, 16, v151
	v_and_b32_e32 v151, 0xffff0000, v151
	v_pk_fma_f32 v[144:145], v[28:29], v[84:85], v[144:145]
	v_pk_fma_f32 v[146:147], v[30:31], v[86:87], v[146:147]
	v_pk_fma_f32 v[148:149], v[20:21], v[80:81], v[148:149]
	v_pk_fma_f32 v[150:151], v[22:23], v[82:83], v[150:151]
	s_mov_b64 s[98:99], 0x8000
	v_lshl_add_u64 v[188:189], v[188:189], 0, s[98:99]
	v_lshl_add_u64 v[176:177], v[188:189], 1, s[12:13]
	v_cvt_pk_bf16_f32 v144, v144, v145
	v_cvt_pk_bf16_f32 v145, v146, v147
	v_cvt_pk_bf16_f32 v146, v148, v149
	v_cvt_pk_bf16_f32 v147, v150, v151
	global_store_dwordx4 v[176:177], v[144:147], off
	s_waitcnt vmcnt(6)
	v_lshlrev_b32_e32 v208, 16, v212
	v_and_b32_e32 v209, 0xffff0000, v212
	v_lshlrev_b32_e32 v210, 16, v213
	v_and_b32_e32 v211, 0xffff0000, v213
	v_lshlrev_b32_e32 v212, 16, v214
	v_and_b32_e32 v213, 0xffff0000, v214
	v_lshlrev_b32_e32 v214, 16, v215
	v_and_b32_e32 v215, 0xffff0000, v215
	v_pk_fma_f32 v[208:209], v[24:25], v[76:77], v[208:209]
	v_pk_fma_f32 v[210:211], v[26:27], v[78:79], v[210:211]
	v_pk_fma_f32 v[212:213], v[16:17], v[68:69], v[212:213]
	v_pk_fma_f32 v[214:215], v[18:19], v[70:71], v[214:215]
	v_cvt_pk_bf16_f32 v208, v208, v209
	v_cvt_pk_bf16_f32 v209, v210, v211
	v_cvt_pk_bf16_f32 v210, v212, v213
	v_cvt_pk_bf16_f32 v211, v214, v215
	global_store_dwordx4 v[176:177], v[208:211], off offset:256
	s_waitcnt vmcnt(5)
	v_lshlrev_b32_e32 v216, 16, v220
	v_and_b32_e32 v217, 0xffff0000, v220
	v_lshlrev_b32_e32 v218, 16, v221
	v_and_b32_e32 v219, 0xffff0000, v221
	v_lshlrev_b32_e32 v220, 16, v222
	v_and_b32_e32 v221, 0xffff0000, v222
	v_lshlrev_b32_e32 v222, 16, v223
	v_and_b32_e32 v223, 0xffff0000, v223
	v_pk_fma_f32 v[216:217], v[8:9], v[84:85], v[216:217]
	v_pk_fma_f32 v[218:219], v[10:11], v[86:87], v[218:219]
	v_pk_fma_f32 v[220:221], v[0:1], v[80:81], v[220:221]
	v_pk_fma_f32 v[222:223], v[2:3], v[82:83], v[222:223]
	s_mov_b64 s[98:99], 0x8000
	v_lshl_add_u64 v[188:189], v[188:189], 0, s[98:99]
	v_lshl_add_u64 v[176:177], v[188:189], 1, s[12:13]
	v_cvt_pk_bf16_f32 v216, v216, v217
	v_cvt_pk_bf16_f32 v217, v218, v219
	v_cvt_pk_bf16_f32 v218, v220, v221
	v_cvt_pk_bf16_f32 v219, v222, v223
	global_store_dwordx4 v[176:177], v[216:219], off
	s_waitcnt vmcnt(4)
	v_lshlrev_b32_e32 v224, 16, v228
	v_and_b32_e32 v225, 0xffff0000, v228
	v_lshlrev_b32_e32 v226, 16, v229
	v_and_b32_e32 v227, 0xffff0000, v229
	v_lshlrev_b32_e32 v228, 16, v230
	v_and_b32_e32 v229, 0xffff0000, v230
	v_lshlrev_b32_e32 v230, 16, v231
	v_and_b32_e32 v231, 0xffff0000, v231
	v_pk_fma_f32 v[224:225], v[12:13], v[76:77], v[224:225]
	v_pk_fma_f32 v[226:227], v[14:15], v[78:79], v[226:227]
	v_pk_fma_f32 v[228:229], v[4:5], v[68:69], v[228:229]
	v_pk_fma_f32 v[230:231], v[6:7], v[70:71], v[230:231]
	v_cvt_pk_bf16_f32 v224, v224, v225
	v_cvt_pk_bf16_f32 v225, v226, v227
	v_cvt_pk_bf16_f32 v226, v228, v229
	v_cvt_pk_bf16_f32 v227, v230, v231
	global_store_dwordx4 v[176:177], v[224:227], off offset:256
	s_branch .LO1_done
.LO1_f32:
	v_mov_b32_e32 v184, v178
	v_mov_b32_e32 v185, v179
	v_mov_b32_e32 v188, v178
	v_mov_b32_e32 v189, v179
	v_lshl_add_u64 v[174:175], v[184:185], 2, s[6:7]
	global_load_dwordx4 v[144:147], v[174:175], off
	global_load_dwordx4 v[148:151], v[174:175], off offset:16
	global_load_dwordx4 v[208:211], v[174:175], off offset:512
	global_load_dwordx4 v[212:215], v[174:175], off offset:528
	s_mov_b64 s[98:99], 0x8000
	v_lshl_add_u64 v[184:185], v[184:185], 0, s[98:99]
	v_lshl_add_u64 v[174:175], v[184:185], 2, s[6:7]
	global_load_dwordx4 v[216:219], v[174:175], off
	global_load_dwordx4 v[220:223], v[174:175], off offset:16
	global_load_dwordx4 v[224:227], v[174:175], off offset:512
	global_load_dwordx4 v[228:231], v[174:175], off offset:528
	s_mov_b64 s[98:99], 0x8000
	v_lshl_add_u64 v[184:185], v[184:185], 0, s[98:99]
	v_lshl_add_u64 v[174:175], v[184:185], 2, s[6:7]
	global_load_dwordx4 v[232:235], v[174:175], off
	global_load_dwordx4 v[236:239], v[174:175], off offset:16
	s_waitcnt vmcnt(8)
	v_pk_fma_f32 v[144:145], v[140:141], v[84:85], v[144:145]
	v_pk_fma_f32 v[146:147], v[142:143], v[86:87], v[146:147]
	v_pk_fma_f32 v[148:149], v[136:137], v[80:81], v[148:149]
	v_pk_fma_f32 v[150:151], v[138:139], v[82:83], v[150:151]
	v_lshl_add_u64 v[176:177], v[188:189], 1, s[12:13]
	v_cvt_pk_bf16_f32 v144, v144, v145
	v_cvt_pk_bf16_f32 v145, v146, v147
	v_cvt_pk_bf16_f32 v146, v148, v149
	v_cvt_pk_bf16_f32 v147, v150, v151
	global_store_dwordx4 v[176:177], v[144:147], off
	global_load_dwordx4 v[240:243], v[174:175], off offset:512
	global_load_dwordx4 v[244:247], v[174:175], off offset:528
	s_waitcnt vmcnt(9)
	v_pk_fma_f32 v[208:209], v[132:133], v[76:77], v[208:209]
	v_pk_fma_f32 v[210:211], v[134:135], v[78:79], v[210:211]
	v_pk_fma_f32 v[212:213], v[128:129], v[68:69], v[212:213]
	v_pk_fma_f32 v[214:215], v[130:131], v[70:71], v[214:215]
	v_cvt_pk_bf16_f32 v208, v208, v209
	v_cvt_pk_bf16_f32 v209, v210, v211
	v_cvt_pk_bf16_f32 v210, v212, v213
	v_cvt_pk_bf16_f32 v211, v214, v215
	global_store_dwordx4 v[176:177], v[208:211], off offset:256
	s_mov_b64 s[98:99], 0x8000
	v_lshl_add_u64 v[184:185], v[184:185], 0, s[98:99]
	v_lshl_add_u64 v[174:175], v[184:185], 2, s[6:7]
	global_load_dwordx4 v[144:147], v[174:175], off
	global_load_dwordx4 v[148:151], v[174:175], off offset:16
	s_waitcnt vmcnt(10)
	v_pk_fma_f32 v[216:217], v[124:125], v[84:85], v[216:217]
	v_pk_fma_f32 v[218:219], v[126:127], v[86:87], v[218:219]
	v_pk_fma_f32 v[220:221], v[120:121], v[80:81], v[220:221]
	v_pk_fma_f32 v[222:223], v[122:123], v[82:83], v[222:223]
	s_mov_b64 s[98:99], 0x8000
	v_lshl_add_u64 v[188:189], v[188:189], 0, s[98:99]
	v_lshl_add_u64 v[176:177], v[188:189], 1, s[12:13]
	v_cvt_pk_bf16_f32 v216, v216, v217
	v_cvt_pk_bf16_f32 v217, v218, v219
	v_cvt_pk_bf16_f32 v218, v220, v221
	v_cvt_pk_bf16_f32 v219, v222, v223
	global_store_dwordx4 v[176:177], v[216:219], off
	global_load_dwordx4 v[208:211], v[174:175], off offset:512
	global_load_dwordx4 v[212:215], v[174:175], off offset:528
	s_waitcnt vmcnt(11)
	v_pk_fma_f32 v[224:225], v[116:117], v[76:77], v[224:225]
	v_pk_fma_f32 v[226:227], v[118:119], v[78:79], v[226:227]
	v_pk_fma_f32 v[228:229], v[112:113], v[68:69], v[228:229]
	v_pk_fma_f32 v[230:231], v[114:115], v[70:71], v[230:231]
	v_cvt_pk_bf16_f32 v224, v224, v225
	v_cvt_pk_bf16_f32 v225, v226, v227
	v_cvt_pk_bf16_f32 v226, v228, v229
	v_cvt_pk_bf16_f32 v227, v230, v231
	global_store_dwordx4 v[176:177], v[224:227], off offset:256
	s_mov_b64 s[98:99], 0x28000
	v_lshl_add_u64 v[184:185], v[184:185], 0, s[98:99]
	v_lshl_add_u64 v[174:175], v[184:185], 2, s[6:7]
	global_load_dwordx4 v[216:219], v[174:175], off
	global_load_dwordx4 v[220:223], v[174:175], off offset:16
	s_waitcnt vmcnt(12)
	v_pk_fma_f32 v[232:233], v[108:109], v[84:85], v[232:233]
	v_pk_fma_f32 v[234:235], v[110:111], v[86:87], v[234:235]
	v_pk_fma_f32 v[236:237], v[104:105], v[80:81], v[236:237]
	v_pk_fma_f32 v[238:239], v[106:107], v[82:83], v[238:239]
	s_mov_b64 s[98:99], 0x8000
	v_lshl_add_u64 v[188:189], v[188:189], 0, s[98:99]
	v_lshl_add_u64 v[176:177], v[188:189], 1, s[12:13]
	v_cvt_pk_bf16_f32 v232, v232, v233
	v_cvt_pk_bf16_f32 v233, v234, v235
	v_cvt_pk_bf16_f32 v234, v236, v237
	v_cvt_pk_bf16_f32 v235, v238, v239
	global_store_dwordx4 v[176:177], v[232:235], off
	global_load_dwordx4 v[224:227], v[174:175], off offset:512
	global_load_dwordx4 v[228:231], v[174:175], off offset:528
	s_waitcnt vmcnt(12)
	v_pk_fma_f32 v[240:241], v[100:101], v[76:77], v[240:241]
	v_pk_fma_f32 v[242:243], v[102:103], v[78:79], v[242:243]
	v_pk_fma_f32 v[244:245], v[96:97], v[68:69], v[244:245]
	v_pk_fma_f32 v[246:247], v[98:99], v[70:71], v[246:247]
	v_cvt_pk_bf16_f32 v240, v240, v241
	v_cvt_pk_bf16_f32 v241, v242, v243
	v_cvt_pk_bf16_f32 v242, v244, v245
	v_cvt_pk_bf16_f32 v243, v246, v247
	global_store_dwordx4 v[176:177], v[240:243], off offset:256
	s_mov_b64 s[98:99], 0x8000
	v_lshl_add_u64 v[184:185], v[184:185], 0, s[98:99]
	v_lshl_add_u64 v[174:175], v[184:185], 2, s[6:7]
	global_load_dwordx4 v[232:235], v[174:175], off
	global_load_dwordx4 v[236:239], v[174:175], off offset:16
	s_waitcnt vmcnt(12)
	v_pk_fma_f32 v[144:145], v[92:93], v[84:85], v[144:145]
	v_pk_fma_f32 v[146:147], v[94:95], v[86:87], v[146:147]
	v_pk_fma_f32 v[148:149], v[88:89], v[80:81], v[148:149]
	v_pk_fma_f32 v[150:151], v[90:91], v[82:83], v[150:151]
	s_mov_b64 s[98:99], 0x8000
	v_lshl_add_u64 v[188:189], v[188:189], 0, s[98:99]
	v_lshl_add_u64 v[176:177], v[188:189], 1, s[12:13]
	v_cvt_pk_bf16_f32 v144, v144, v145
	v_cvt_pk_bf16_f32 v145, v146, v147
	v_cvt_pk_bf16_f32 v146, v148, v149
	v_cvt_pk_bf16_f32 v147, v150, v151
	global_store_dwordx4 v[176:177], v[144:147], off
	global_load_dwordx4 v[240:243], v[174:175], off offset:512
	global_load_dwordx4 v[244:247], v[174:175], off offset:528
	s_waitcnt vmcnt(12)
	v_pk_fma_f32 v[208:209], v[72:73], v[76:77], v[208:209]
	v_pk_fma_f32 v[210:211], v[74:75], v[78:79], v[210:211]
	v_pk_fma_f32 v[212:213], v[64:65], v[68:69], v[212:213]
	v_pk_fma_f32 v[214:215], v[66:67], v[70:71], v[214:215]
	v_cvt_pk_bf16_f32 v208, v208, v209
	v_cvt_pk_bf16_f32 v209, v210, v211
	v_cvt_pk_bf16_f32 v210, v212, v213
	v_cvt_pk_bf16_f32 v211, v214, v215
	global_store_dwordx4 v[176:177], v[208:211], off offset:256
	s_mov_b64 s[98:99], 0x8000
	v_lshl_add_u64 v[184:185], v[184:185], 0, s[98:99]
	v_lshl_add_u64 v[174:175], v[184:185], 2, s[6:7]
	global_load_dwordx4 v[144:147], v[174:175], off
	global_load_dwordx4 v[148:151], v[174:175], off offset:16
	s_waitcnt vmcnt(12)
	v_pk_fma_f32 v[216:217], v[60:61], v[84:85], v[216:217]
	v_pk_fma_f32 v[218:219], v[62:63], v[86:87], v[218:219]
	v_pk_fma_f32 v[220:221], v[56:57], v[80:81], v[220:221]
	v_pk_fma_f32 v[222:223], v[58:59], v[82:83], v[222:223]
	s_mov_b64 s[98:99], 0x28000
	v_lshl_add_u64 v[188:189], v[188:189], 0, s[98:99]
	v_lshl_add_u64 v[176:177], v[188:189], 1, s[12:13]
	v_cvt_pk_bf16_f32 v216, v216, v217
	v_cvt_pk_bf16_f32 v217, v218, v219
	v_cvt_pk_bf16_f32 v218, v220, v221
	v_cvt_pk_bf16_f32 v219, v222, v223
	global_store_dwordx4 v[176:177], v[216:219], off
	global_load_dwordx4 v[208:211], v[174:175], off offset:512
	global_load_dwordx4 v[212:215], v[174:175], off offset:528
	s_waitcnt vmcnt(12)
	v_pk_fma_f32 v[224:225], v[52:53], v[76:77], v[224:225]
	v_pk_fma_f32 v[226:227], v[54:55], v[78:79], v[226:227]
	v_pk_fma_f32 v[228:229], v[48:49], v[68:69], v[228:229]
	v_pk_fma_f32 v[230:231], v[50:51], v[70:71], v[230:231]
	v_cvt_pk_bf16_f32 v224, v224, v225
	v_cvt_pk_bf16_f32 v225, v226, v227
	v_cvt_pk_bf16_f32 v226, v228, v229
	v_cvt_pk_bf16_f32 v227, v230, v231
	global_store_dwordx4 v[176:177], v[224:227], off offset:256
	s_mov_b64 s[98:99], 0x8000
	v_lshl_add_u64 v[184:185], v[184:185], 0, s[98:99]
	v_lshl_add_u64 v[174:175], v[184:185], 2, s[6:7]
	global_load_dwordx4 v[216:219], v[174:175], off
	global_load_dwordx4 v[220:223], v[174:175], off offset:16
	s_waitcnt vmcnt(12)
	v_pk_fma_f32 v[232:233], v[44:45], v[84:85], v[232:233]
	v_pk_fma_f32 v[234:235], v[46:47], v[86:87], v[234:235]
	v_pk_fma_f32 v[236:237], v[40:41], v[80:81], v[236:237]
	v_pk_fma_f32 v[238:239], v[42:43], v[82:83], v[238:239]
	s_mov_b64 s[98:99], 0x8000
	v_lshl_add_u64 v[188:189], v[188:189], 0, s[98:99]
	v_lshl_add_u64 v[176:177], v[188:189], 1, s[12:13]
	v_cvt_pk_bf16_f32 v232, v232, v233
	v_cvt_pk_bf16_f32 v233, v234, v235
	v_cvt_pk_bf16_f32 v234, v236, v237
	v_cvt_pk_bf16_f32 v235, v238, v239
	global_store_dwordx4 v[176:177], v[232:235], off
	global_load_dwordx4 v[224:227], v[174:175], off offset:512
	global_load_dwordx4 v[228:231], v[174:175], off offset:528
	s_waitcnt vmcnt(12)
	v_pk_fma_f32 v[240:241], v[36:37], v[76:77], v[240:241]
	v_pk_fma_f32 v[242:243], v[38:39], v[78:79], v[242:243]
	v_pk_fma_f32 v[244:245], v[32:33], v[68:69], v[244:245]
	v_pk_fma_f32 v[246:247], v[34:35], v[70:71], v[246:247]
	v_cvt_pk_bf16_f32 v240, v240, v241
	v_cvt_pk_bf16_f32 v241, v242, v243
	v_cvt_pk_bf16_f32 v242, v244, v245
	v_cvt_pk_bf16_f32 v243, v246, v247
	global_store_dwordx4 v[176:177], v[240:243], off offset:256
	s_waitcnt vmcnt(10)
	v_pk_fma_f32 v[144:145], v[28:29], v[84:85], v[144:145]
	v_pk_fma_f32 v[146:147], v[30:31], v[86:87], v[146:147]
	v_pk_fma_f32 v[148:149], v[20:21], v[80:81], v[148:149]
	v_pk_fma_f32 v[150:151], v[22:23], v[82:83], v[150:151]
	s_mov_b64 s[98:99], 0x8000
	v_lshl_add_u64 v[188:189], v[188:189], 0, s[98:99]
	v_lshl_add_u64 v[176:177], v[188:189], 1, s[12:13]
	v_cvt_pk_bf16_f32 v144, v144, v145
	v_cvt_pk_bf16_f32 v145, v146, v147
	v_cvt_pk_bf16_f32 v146, v148, v149
	v_cvt_pk_bf16_f32 v147, v150, v151
	global_store_dwordx4 v[176:177], v[144:147], off
	s_waitcnt vmcnt(8)
	v_pk_fma_f32 v[208:209], v[24:25], v[76:77], v[208:209]
	v_pk_fma_f32 v[210:211], v[26:27], v[78:79], v[210:211]
	v_pk_fma_f32 v[212:213], v[16:17], v[68:69], v[212:213]
	v_pk_fma_f32 v[214:215], v[18:19], v[70:71], v[214:215]
	v_cvt_pk_bf16_f32 v208, v208, v209
	v_cvt_pk_bf16_f32 v209, v210, v211
	v_cvt_pk_bf16_f32 v210, v212, v213
	v_cvt_pk_bf16_f32 v211, v214, v215
	global_store_dwordx4 v[176:177], v[208:211], off offset:256
	s_waitcnt vmcnt(6)
	v_pk_fma_f32 v[216:217], v[8:9], v[84:85], v[216:217]
	v_pk_fma_f32 v[218:219], v[10:11], v[86:87], v[218:219]
	v_pk_fma_f32 v[220:221], v[0:1], v[80:81], v[220:221]
	v_pk_fma_f32 v[222:223], v[2:3], v[82:83], v[222:223]
	s_mov_b64 s[98:99], 0x8000
	v_lshl_add_u64 v[188:189], v[188:189], 0, s[98:99]
	v_lshl_add_u64 v[176:177], v[188:189], 1, s[12:13]
	v_cvt_pk_bf16_f32 v216, v216, v217
	v_cvt_pk_bf16_f32 v217, v218, v219
	v_cvt_pk_bf16_f32 v218, v220, v221
	v_cvt_pk_bf16_f32 v219, v222, v223
	global_store_dwordx4 v[176:177], v[216:219], off
	s_waitcnt vmcnt(4)
	v_pk_fma_f32 v[224:225], v[12:13], v[76:77], v[224:225]
	v_pk_fma_f32 v[226:227], v[14:15], v[78:79], v[226:227]
	v_pk_fma_f32 v[228:229], v[4:5], v[68:69], v[228:229]
	v_pk_fma_f32 v[230:231], v[6:7], v[70:71], v[230:231]
	v_cvt_pk_bf16_f32 v224, v224, v225
	v_cvt_pk_bf16_f32 v225, v226, v227
	v_cvt_pk_bf16_f32 v226, v228, v229
	v_cvt_pk_bf16_f32 v227, v230, v231
	global_store_dwordx4 v[176:177], v[224:227], off offset:256
.LO1_done:
	s_andn2_b64 vcc, exec, s[0:1]
	s_mov_b64 s[0:1], -1
	s_cbranch_vccnz .LBB0_994
	s_andn2_b64 vcc, exec, s[2:3]
	s_cbranch_vccnz .LBB0_993
	s_barrier
	s_branch .LBB0_993
